# DSA indexer scoring loop: one permlane16 swap+add sums two query pairs at once (all lanes store), two key-tile register sets with prefetch two tiles ahead instead of register copies
# speedup vs baseline: 1.0084x; 1.0079x over previous
.LBB0_721:
	s_or_b64 exec, exec, s[0:1]
	s_lshl_b64 s[0:1], s[4:5], 6
	s_cmpk_lt_u32 s6, 0x100
	v_writelane_b32 v254, s0, 48
	s_cselect_b64 s[4:5], -1, 0
	s_and_b64 vcc, exec, s[4:5]
	v_writelane_b32 v254, s1, 49
	s_cbranch_vccnz .LBB0_738
	s_lshr_b32 s7, s6, 4
	v_readlane_b32 s0, v254, 29
	v_readlane_b32 s10, v254, 34
	s_cmp_gt_i32 s0, s7
	v_readlane_b32 s11, v254, 35
	s_cbranch_scc1 .LBB0_725
	s_waitcnt vmcnt(2)
	v_lshlrev_b32_e32 v56, 16, v174
	v_and_b32_e32 v57, 0xffff0000, v174
	s_mov_b32 s0, 0x3eb504f3
	v_pk_mul_f32 v[64:65], v[56:57], s[0:1] op_sel_hi:[1,0]
	v_and_b32_e32 v56, 0xffff0000, v175
	v_lshlrev_b32_e32 v57, 16, v175
	v_pk_mul_f32 v[66:67], v[56:57], s[0:1] op_sel_hi:[1,0]
	v_lshlrev_b32_e32 v56, 16, v172
	v_and_b32_e32 v57, 0xffff0000, v172
	v_pk_mul_f32 v[68:69], v[56:57], s[0:1] op_sel_hi:[1,0]
	v_and_b32_e32 v56, 0xffff0000, v173
	v_lshlrev_b32_e32 v57, 16, v173
	v_pk_mul_f32 v[70:71], v[56:57], s[0:1] op_sel_hi:[1,0]
	v_lshlrev_b32_e32 v56, 16, v170
	v_and_b32_e32 v57, 0xffff0000, v170
	v_pk_mul_f32 v[72:73], v[56:57], s[0:1] op_sel_hi:[1,0]
	v_and_b32_e32 v56, 0xffff0000, v171
	v_lshlrev_b32_e32 v57, 16, v171
	v_pk_mul_f32 v[74:75], v[56:57], s[0:1] op_sel_hi:[1,0]
	v_lshlrev_b32_e32 v56, 16, v168
	v_and_b32_e32 v57, 0xffff0000, v168
	v_pk_mul_f32 v[76:77], v[56:57], s[0:1] op_sel_hi:[1,0]
	v_and_b32_e32 v56, 0xffff0000, v169
	v_lshlrev_b32_e32 v57, 16, v169
	v_pk_mul_f32 v[78:79], v[56:57], s[0:1] op_sel_hi:[1,0]
	v_or_b32_e32 v56, 2, v1
	v_readlane_b32 s0, v254, 48
	s_waitcnt vmcnt(1)
	v_or_b32_e32 v83, s6, v56
	v_or_b32_e32 v56, 4, v1
	v_readlane_b32 s1, v254, 49
	s_waitcnt vmcnt(0)
	v_or_b32_e32 v84, s6, v56
	v_or_b32_e32 v56, 6, v1
	v_lshl_add_u64 v[80:81], s[0:1], 1, v[156:157]
	v_or_b32_e32 v82, s6, v1
	v_or_b32_e32 v85, s6, v56
	v_mov_b32_e32 v86, v231
	v_mov_b32_e32 v87, v230
	v_readlane_b32 s0, v254, 29
	v_add_u32_e32 v133, 0xfffe8000, v86
	v_add_u32_e32 v134, 0xffff8000, v86
	v_bfe_u32 v124, v152, 4, 1
	v_lshlrev_b32_e32 v125, 1, v124
	v_or_b32_e32 v82, v82, v125
	v_or_b32_e32 v83, 4, v82
	v_lshl_add_u32 v133, v124, 15, v133
	v_add_u32_e32 v134, 0x10000, v133
	s_mov_b32 s21, 0x80000000
	s_add_i32 s9, s0, 8
	s_cmp_gt_i32 s9, s7
	s_cselect_b32 s9, s0, s9
	s_lshl_b32 s2, s9, 4
	s_ashr_i32 s3, s2, 31
	s_lshl_b64 s[2:3], s[2:3], 7
	v_lshl_add_u64 v[60:61], v[80:81], 0, s[2:3]
	global_load_dwordx4 v[56:59], v[60:61], off
	s_nop 0
	global_load_dwordx4 v[60:63], v[60:61], off offset:1024
.LBB0_724:
	s_add_i32 s8, s0, 8
	s_cmp_gt_i32 s8, s7
	s_cselect_b64 s[2:3], -1, 0
	s_and_b64 vcc, s[2:3], exec
	s_add_i32 s9, s0, 16
	s_cmp_gt_i32 s9, s7
	s_cselect_b32 s0, s0, s9
	s_lshl_b32 s0, s0, 4
	s_ashr_i32 s1, s0, 31
	s_lshl_b64 s[0:1], s[0:1], 7
	s_waitcnt vmcnt(2)
	v_mfma_f32_16x16x32_bf16 v[100:103], v[28:31], v[44:47], 0
	v_mfma_f32_16x16x32_bf16 v[104:107], v[32:35], v[44:47], 0
	v_mfma_f32_16x16x32_bf16 v[108:111], v[24:27], v[44:47], 0
	v_mfma_f32_16x16x32_bf16 v[112:115], v[36:39], v[44:47], 0
	v_mfma_f32_16x16x32_bf16 v[100:103], v[20:23], v[40:43], v[100:103]
	v_mfma_f32_16x16x32_bf16 v[104:107], v[12:15], v[40:43], v[104:107]
	v_mfma_f32_16x16x32_bf16 v[108:111], v[16:19], v[40:43], v[108:111]
	v_mfma_f32_16x16x32_bf16 v[112:115], v[8:11], v[40:43], v[112:115]
	s_nop 4
	v_max_f32_e32 v100, 0, v100
	v_max_f32_e32 v101, 0, v101
	v_max_f32_e32 v102, 0, v102
	v_max_f32_e32 v103, 0, v103
	v_mul_f32_e32 v116, v65, v101
	v_fma_f32 v116, v64, v100, v116
	v_mul_f32_e32 v117, v67, v102
	v_add_f32_e32 v116, v117, v116
	v_fma_f32 v116, v66, v103, v116
	v_lshl_add_u64 v[40:41], v[80:81], 0, s[0:1]
	global_load_dwordx4 v[44:47], v[40:41], off
	s_nop 0
	global_load_dwordx4 v[40:43], v[40:41], off offset:1024
	v_max_f32_e32 v104, 0, v104
	v_max_f32_e32 v105, 0, v105
	v_max_f32_e32 v106, 0, v106
	v_max_f32_e32 v107, 0, v107
	v_mul_f32_e32 v118, v69, v105
	v_fma_f32 v118, v68, v104, v118
	v_mul_f32_e32 v119, v71, v106
	v_add_f32_e32 v118, v119, v118
	v_fma_f32 v118, v70, v107, v118
	v_max_f32_e32 v108, 0, v108
	v_max_f32_e32 v109, 0, v109
	v_max_f32_e32 v110, 0, v110
	v_max_f32_e32 v111, 0, v111
	v_mul_f32_e32 v120, v73, v109
	v_fma_f32 v120, v72, v108, v120
	v_mul_f32_e32 v121, v75, v110
	v_add_f32_e32 v120, v121, v120
	v_fma_f32 v120, v74, v111, v120
	v_max_f32_e32 v112, 0, v112
	v_max_f32_e32 v113, 0, v113
	v_max_f32_e32 v114, 0, v114
	v_max_f32_e32 v115, 0, v115
	v_mul_f32_e32 v122, v77, v113
	v_fma_f32 v122, v76, v112, v122
	v_mul_f32_e32 v123, v79, v114
	v_add_f32_e32 v122, v123, v122
	v_fma_f32 v122, v78, v115, v122
	v_cmp_le_i32_e64 s[24:25], v87, v82
	v_cmp_le_i32_e64 s[26:27], v87, v83
	v_permlane16_swap_b32_e32 v116, v118
	v_permlane16_swap_b32_e32 v120, v122
	v_add_f32_e32 v116, v116, v118
	v_add_f32_e32 v120, v120, v122
	v_ashrrev_i32_e32 v124, 31, v116
	v_ashrrev_i32_e32 v126, 31, v120
	v_bitop3_b32 v116, v116, v124, s21 bitop3:0x1e
	v_bitop3_b32 v120, v120, v126, s21 bitop3:0x1e
	v_cndmask_b32_e64 v116, 0, v116, s[24:25]
	v_cndmask_b32_e64 v120, 0, v120, s[26:27]
	ds_write_b32 v133, v116
	ds_write_b32 v134, v120
	v_add_u32_e32 v133, 0x200, v133
	v_add_u32_e32 v134, 0x200, v134
	v_add_u32_e32 v87, 0x80, v87
	s_mov_b32 s0, s8
	s_cbranch_vccnz .Lsc_exit
.Lsc_B:
	s_add_i32 s8, s0, 8
	s_cmp_gt_i32 s8, s7
	s_cselect_b64 s[2:3], -1, 0
	s_and_b64 vcc, s[2:3], exec
	s_add_i32 s9, s0, 16
	s_cmp_gt_i32 s9, s7
	s_cselect_b32 s0, s0, s9
	s_lshl_b32 s0, s0, 4
	s_ashr_i32 s1, s0, 31
	s_lshl_b64 s[0:1], s[0:1], 7
	s_waitcnt vmcnt(2)
	v_mfma_f32_16x16x32_bf16 v[100:103], v[28:31], v[56:59], 0
	v_mfma_f32_16x16x32_bf16 v[104:107], v[32:35], v[56:59], 0
	v_mfma_f32_16x16x32_bf16 v[108:111], v[24:27], v[56:59], 0
	v_mfma_f32_16x16x32_bf16 v[112:115], v[36:39], v[56:59], 0
	v_mfma_f32_16x16x32_bf16 v[100:103], v[20:23], v[60:63], v[100:103]
	v_mfma_f32_16x16x32_bf16 v[104:107], v[12:15], v[60:63], v[104:107]
	v_mfma_f32_16x16x32_bf16 v[108:111], v[16:19], v[60:63], v[108:111]
	v_mfma_f32_16x16x32_bf16 v[112:115], v[8:11], v[60:63], v[112:115]
	s_nop 4
	v_max_f32_e32 v100, 0, v100
	v_max_f32_e32 v101, 0, v101
	v_max_f32_e32 v102, 0, v102
	v_max_f32_e32 v103, 0, v103
	v_mul_f32_e32 v116, v65, v101
	v_fma_f32 v116, v64, v100, v116
	v_mul_f32_e32 v117, v67, v102
	v_add_f32_e32 v116, v117, v116
	v_fma_f32 v116, v66, v103, v116
	v_lshl_add_u64 v[60:61], v[80:81], 0, s[0:1]
	global_load_dwordx4 v[56:59], v[60:61], off
	s_nop 0
	global_load_dwordx4 v[60:63], v[60:61], off offset:1024
	v_max_f32_e32 v104, 0, v104
	v_max_f32_e32 v105, 0, v105
	v_max_f32_e32 v106, 0, v106
	v_max_f32_e32 v107, 0, v107
	v_mul_f32_e32 v118, v69, v105
	v_fma_f32 v118, v68, v104, v118
	v_mul_f32_e32 v119, v71, v106
	v_add_f32_e32 v118, v119, v118
	v_fma_f32 v118, v70, v107, v118
	v_max_f32_e32 v108, 0, v108
	v_max_f32_e32 v109, 0, v109
	v_max_f32_e32 v110, 0, v110
	v_max_f32_e32 v111, 0, v111
	v_mul_f32_e32 v120, v73, v109
	v_fma_f32 v120, v72, v108, v120
	v_mul_f32_e32 v121, v75, v110
	v_add_f32_e32 v120, v121, v120
	v_fma_f32 v120, v74, v111, v120
	v_max_f32_e32 v112, 0, v112
	v_max_f32_e32 v113, 0, v113
	v_max_f32_e32 v114, 0, v114
	v_max_f32_e32 v115, 0, v115
	v_mul_f32_e32 v122, v77, v113
	v_fma_f32 v122, v76, v112, v122
	v_mul_f32_e32 v123, v79, v114
	v_add_f32_e32 v122, v123, v122
	v_fma_f32 v122, v78, v115, v122
	v_cmp_le_i32_e64 s[24:25], v87, v82
	v_cmp_le_i32_e64 s[26:27], v87, v83
	v_permlane16_swap_b32_e32 v116, v118
	v_permlane16_swap_b32_e32 v120, v122
	v_add_f32_e32 v116, v116, v118
	v_add_f32_e32 v120, v120, v122
	v_ashrrev_i32_e32 v124, 31, v116
	v_ashrrev_i32_e32 v126, 31, v120
	v_bitop3_b32 v116, v116, v124, s21 bitop3:0x1e
	v_bitop3_b32 v120, v120, v126, s21 bitop3:0x1e
	v_cndmask_b32_e64 v116, 0, v116, s[24:25]
	v_cndmask_b32_e64 v120, 0, v120, s[26:27]
	ds_write_b32 v133, v116
	ds_write_b32 v134, v120
	v_add_u32_e32 v133, 0x200, v133
	v_add_u32_e32 v134, 0x200, v134
	v_add_u32_e32 v87, 0x80, v87
	s_mov_b32 s0, s8
	s_cbranch_vccz .LBB0_724
.Lsc_exit:
	s_waitcnt vmcnt(0)
.LBB0_725:
	s_mov_b64 s[2:3], exec
	v_readlane_b32 s0, v254, 36
	v_readlane_b32 s1, v254, 37
	s_and_b64 s[0:1], s[2:3], s[0:1]
	s_mov_b64 exec, s[0:1]
	s_cbranch_execz .LBB0_737
	s_and_b32 s0, s6, 0xff0
	s_addk_i32 s6, 0x207
	s_waitcnt vmcnt(4)
	v_add_u32_e32 v8, 16, v182
	s_and_b32 s1, s6, 0x1e00
	v_add_u32_e32 v8, s0, v8
	v_cmp_gt_u32_e32 vcc, s1, v8
	v_add_u32_e32 v8, s0, v182
	v_lshl_add_u32 v10, v8, 2, 0
	s_mov_b64 s[0:1], -1
	v_mov_b32_e32 v9, v152
	s_mov_b64 s[6:7], exec
	v_readlane_b32 s8, v254, 42
	v_readlane_b32 s9, v254, 43
	s_and_b64 s[8:9], s[6:7], s[8:9]
	s_mov_b64 exec, s[8:9]
	s_cbranch_execz .LBB0_732
	s_mov_b64 s[8:9], 0
	v_mov_b32_e32 v11, v245
	v_mov_b64_e32 v[8:9], v[152:153]
	s_branch .LBB0_729
